# speedup vs baseline: 1.0059x; 1.0050x over previous
_Z9attn_mfmaPKtS0_PKfS2_PtS3_S3_:
	s_load_dwordx2 s[10:11], s[0:1], 0x18
	s_load_dwordx2 s[36:37], s[0:1], 0x10
	s_load_dwordx4 s[4:7], s[0:1], 0x0
	s_load_dwordx2 s[8:9], s[0:1], 0x20
	s_load_dwordx4 s[24:27], s[0:1], 0x28
	s_bfe_u32 s28, s2, 0x30003
	v_and_b32_e32 v157, 31, v0
	v_readfirstlane_b32 s29, v0
	s_and_b32 s12, s2, 7
	s_ashr_i32 s2, s2, 3
	s_and_b32 s13, s2, -8
	s_or_b32 s30, s13, s12
	v_lshlrev_b32_e32 v201, 3, v0
	v_and_b32_e32 v201, 0x300, v201
	s_lshl_b32 s3, s28, 5
	v_or3_b32 v201, s3, v201, v157
	v_lshlrev_b32_e32 v201, 2, v201
	v_cmp_gt_u32_e32 vcc, 0x60, v0
	s_waitcnt lgkmcnt(0)
	s_and_saveexec_b64 s[38:39], vcc
	global_load_dword v200, v201, s[36:37]
	s_mov_b64 exec, s[38:39]
	s_cmpk_lt_u32 s29, 0x100
	s_cbranch_scc1 .Lmy_ps_lo
	s_lshl_b32 s14, s12, 11
	v_or_b32_sdwa v201, s14, v0 dst_sel:DWORD dst_unused:UNUSED_PAD src0_sel:DWORD src1_sel:BYTE_0
	v_lshlrev_b32_e32 v202, 2, v201
	v_mov_b32_e32 v203, 0
	v_lshl_add_u64 v[204:205], s[10:11], 0, v[202:203]
	v_or_b32_e32 v201, s14, v0
	s_movk_i32 s14, 0x1000
	v_add_co_u32_e32 v206, vcc, s14, v204
	s_mov_b32 s14, 0x10000
	s_nop 0
	v_addc_co_u32_e32 v207, vcc, 0, v205, vcc
	v_add_co_u32_e32 v208, vcc, s14, v204
	v_lshlrev_b32_e32 v201, 2, v201
	s_nop 0
	v_addc_co_u32_e32 v209, vcc, 0, v205, vcc
	s_mov_b32 s14, 0x11000
	v_or_b32_e32 v203, 0xc00, v201
	v_add_co_u32_e32 v210, vcc, s14, v204
	v_or_b32_e32 v212, 0x1c00, v201
	s_nop 0
	v_addc_co_u32_e32 v211, vcc, 0, v205, vcc
	v_or_b32_e32 v213, 0x10c00, v201
	global_load_dword v214, v203, s[10:11]
	global_load_dword v215, v[206:207], off
	global_load_dword v216, v[206:207], off offset:1024
	global_load_dword v217, v[206:207], off offset:2048
	global_load_dword v218, v212, s[10:11]
	global_load_dword v219, v[208:209], off offset:1024
	global_load_dword v220, v[208:209], off offset:2048
	global_load_dword v221, v213, s[10:11]
	global_load_dword v222, v202, s[10:11]
	global_load_dword v223, v202, s[10:11] offset:1024
	global_load_dword v224, v202, s[10:11] offset:2048
	global_load_dword v225, v[210:211], off offset:-4096
	global_load_dword v226, v[210:211], off
	global_load_dword v227, v[210:211], off offset:1024
	global_load_dword v228, v[210:211], off offset:2048
	s_mov_b32 s14, 0x20000
	v_add_co_u32_e32 v202, vcc, s14, v204
	s_mov_b32 s14, 0x21000
	s_nop 0
	v_addc_co_u32_e32 v203, vcc, 0, v205, vcc
	v_add_co_u32_e32 v206, vcc, s14, v204
	v_or_b32_e32 v208, 0x11c00, v201
	s_nop 0
	v_addc_co_u32_e32 v207, vcc, 0, v205, vcc
	global_load_dword v209, v[206:207], off offset:-4096
	v_or_b32_e32 v210, 0x20c00, v201
	global_load_dword v211, v208, s[10:11]
	global_load_dword v212, v[202:203], off offset:1024
	global_load_dword v213, v[202:203], off offset:2048
	global_load_dword v229, v210, s[10:11]
	s_mov_b32 s14, 0x30000
	v_add_co_u32_e32 v202, vcc, s14, v204
	s_mov_b32 s14, 0x31000
	s_nop 0
	v_addc_co_u32_e32 v203, vcc, 0, v205, vcc
	v_add_co_u32_e32 v204, vcc, s14, v204
	v_or_b32_e32 v208, 0x21c00, v201
	s_nop 0
	v_addc_co_u32_e32 v205, vcc, 0, v205, vcc
	global_load_dword v210, v[206:207], off
	global_load_dword v230, v[206:207], off offset:1024
	global_load_dword v231, v[206:207], off offset:2048
	global_load_dword v232, v[204:205], off offset:-4096
	v_or_b32_e32 v206, 0x30c00, v201
	global_load_dword v207, v208, s[10:11]
	global_load_dword v233, v[202:203], off offset:1024
	global_load_dword v234, v[202:203], off offset:2048
	global_load_dword v235, v206, s[10:11]
	global_load_dword v236, v[204:205], off
	global_load_dword v237, v[204:205], off offset:1024
	global_load_dword v238, v[204:205], off offset:2048
	v_or_b32_e32 v201, 0x31c00, v201
	global_load_dword v201, v201, s[10:11]
	s_branch .Lmy_ps_done
.Lmy_ps_lo:
	v_lshl_or_b32 v202, s30, 11, v0
	v_ashrrev_i32_e32 v203, 31, v202
	v_lshl_add_u64 v[202:203], v[202:203], 2, s[10:11]
	v_add_co_u32_e32 v204, vcc, 0x1000, v202
	s_nop 1
	v_addc_co_u32_e32 v205, vcc, 0, v203, vcc
	global_load_dword v201, v[202:203], off
	global_load_dword v206, v[202:203], off offset:1024
	global_load_dword v207, v[202:203], off offset:2048
	global_load_dword v208, v[202:203], off offset:3072
	global_load_dword v209, v[204:205], off
	global_load_dword v210, v[204:205], off offset:1024
	global_load_dword v211, v[204:205], off offset:2048
	global_load_dword v212, v[204:205], off offset:3072
.Lmy_ps_done:
	s_lshl_b32 s0, s30, 3
	v_mov_b32_e32 v159, 0
	s_or_b32 s0, s0, s28
	s_lshr_b32 s31, s29, 6
	s_mul_hi_i32 s1, s0, 0x10800
	s_mul_i32 s0, s0, 0x10800
	s_waitcnt lgkmcnt(0)
	s_add_u32 s0, s8, s0
	s_addc_u32 s1, s9, s1
	s_lshl_b32 s2, s28, 3
	s_mov_b32 s3, 0
	s_add_i32 s2, s31, s2
	s_lshl_b64 s[8:9], s[2:3], 10
	s_add_u32 s8, s6, s8
	v_and_b32_e32 v154, 63, v0
	s_addc_u32 s9, s7, s9
	s_lshl_b32 s10, s31, 10
	v_lshlrev_b32_e32 v158, 4, v154
	s_add_i32 m0, s10, 0x21a00
	s_addk_i32 s2, 0x80
	global_load_lds_dwordx4 v158, s[8:9]
	s_lshl_b64 s[8:9], s[2:3], 10
	s_add_u32 s8, s6, s8
	s_addc_u32 s9, s7, s9
	v_lshl_add_u64 v[2:3], s[6:7], 0, v[158:159]
	s_lshl_b32 s2, s28, 13
	v_lshl_add_u64 v[2:3], v[2:3], 0, s[2:3]
	s_mov_b32 s2, 0x10000
	v_add_co_u32_e32 v4, vcc, s2, v2
	s_add_i32 m0, s10, 0x23a00
	s_nop 0
	v_addc_co_u32_e32 v5, vcc, 0, v3, vcc
	s_mov_b32 s2, 0x11000
	s_mul_i32 s6, s30, 0x42000
	v_add_co_u32_e32 v2, vcc, s2, v2
	s_mul_hi_i32 s2, s30, 0x42000
	s_add_u32 s4, s4, s6
	global_load_lds_dwordx4 v158, s[8:9]
	s_addc_u32 s5, s5, s2
	s_lshl_b32 s6, s31, 2
	s_mov_b32 s7, s3
	v_addc_co_u32_e32 v3, vcc, 0, v3, vcc
	global_load_dwordx4 v[60:63], v[4:5], off offset:1024
	global_load_dwordx4 v[40:43], v[4:5], off offset:2048
	global_load_dwordx4 v[44:47], v[4:5], off offset:3072
	global_load_dwordx4 v[56:59], v[2:3], off offset:-4096
	global_load_dwordx4 v[48:51], v[2:3], off
	global_load_dwordx4 v[52:55], v[2:3], off offset:1024
	global_load_dwordx4 v[32:35], v[2:3], off offset:2048
	global_load_dwordx4 v[36:39], v[2:3], off offset:3072
	v_lshl_add_u64 v[152:153], s[4:5], 0, v[158:159]
	s_lshl_b64 s[4:5], s[6:7], 13
	v_lshl_add_u64 v[2:3], v[152:153], 0, s[4:5]
	s_movk_i32 s5, 0x1000
	global_load_dwordx4 v[88:91], v[2:3], off
	global_load_dwordx4 v[92:95], v[2:3], off offset:1024
	global_load_dwordx4 v[72:75], v[2:3], off offset:2048
	global_load_dwordx4 v[76:79], v[2:3], off offset:3072
	v_add_co_u32_e32 v2, vcc, s5, v2
	v_bfe_u32 v164, v0, 5, 1
	s_nop 0
	v_addc_co_u32_e32 v3, vcc, 0, v3, vcc
	global_load_dwordx4 v[80:83], v[2:3], off
	global_load_dwordx4 v[84:87], v[2:3], off offset:1024
	global_load_dwordx4 v[64:67], v[2:3], off offset:2048
	global_load_dwordx4 v[68:71], v[2:3], off offset:3072
	s_waitcnt vmcnt(18)
	s_cmpk_lt_u32 s29, 0x100
	s_cbranch_scc1 .Lmy_sum_lo
	v_add_f32_e32 v202, 0, v222
	v_add_f32_e32 v202, v202, v223
	v_add_f32_e32 v202, v202, v224
	v_add_f32_e32 v202, v202, v214
	v_add_f32_e32 v202, v202, v215
	v_add_f32_e32 v202, v202, v216
	v_add_f32_e32 v202, v202, v217
	v_add_f32_e32 v202, v202, v218
	v_add_f32_e32 v202, v202, v225
	v_add_f32_e32 v202, v202, v219
	v_add_f32_e32 v202, v202, v220
	v_add_f32_e32 v202, v202, v221
	v_add_f32_e32 v202, v202, v226
	v_add_f32_e32 v202, v202, v227
	v_add_f32_e32 v202, v202, v228
	v_add_f32_e32 v202, v202, v211
	v_add_f32_e32 v202, v202, v209
	v_add_f32_e32 v202, v202, v212
	v_add_f32_e32 v202, v202, v213
	v_add_f32_e32 v202, v202, v229
	v_add_f32_e32 v202, v202, v210
	v_add_f32_e32 v202, v202, v230
	v_add_f32_e32 v202, v202, v231
	v_add_f32_e32 v202, v202, v207
	v_add_f32_e32 v202, v202, v232
	v_add_f32_e32 v202, v202, v233
	v_add_f32_e32 v202, v202, v234
	v_add_f32_e32 v202, v202, v235
	v_add_f32_e32 v202, v202, v236
	v_add_f32_e32 v202, v202, v237
	v_add_f32_e32 v202, v202, v238
	v_add_f32_e32 v201, v202, v201
	v_mul_f32_e32 v201, 0x39800000, v201
	s_branch .Lmy_sum_done
.Lmy_sum_lo:
	v_add_f32_e32 v201, 0, v201
	v_add_f32_e32 v201, v201, v206
	v_add_f32_e32 v201, v201, v207
	v_add_f32_e32 v201, v201, v208
	v_add_f32_e32 v201, v201, v209
	v_add_f32_e32 v201, v201, v210
	v_add_f32_e32 v201, v201, v211
	v_add_f32_e32 v201, v201, v212
	v_mul_f32_e32 v201, 0x3a800000, v201
.Lmy_sum_done:
	v_mov_b32_e32 v202, 0
	v_cvt_pk_fp8_f32 v202, v201, 0
	v_cvt_pk_fp8_f32 v202, 0, 0 op_sel:[0,0,1]
	s_nop 0
	v_or_b32_e32 v203, 0x25c00, v0
	ds_write_b8 v203, v202
	v_cmp_gt_u32_e32 vcc, 0x60, v0
	s_and_saveexec_b64 s[38:39], vcc
	v_mov_b32_e32 v204, 0x25a00
	v_lshl_add_u32 v204, v0, 2, v204
	ds_write_b32 v204, v200
	s_mov_b64 exec, s[38:39]
	s_waitcnt vmcnt(0)
	v_lshlrev_b32_e32 v0, 4, v164
	v_mov_b32_e32 v1, 0x25a00
	v_lshlrev_b32_e32 v156, 3, v154
	v_lshl_add_u64 v[160:161], s[0:1], 0, v[158:159]
	v_or_b32_e32 v162, 0x25a80, v0
	v_lshl_or_b32 v155, v157, 2, v1
	v_or_b32_e32 v163, 0x25a00, v0
	v_or_b32_e32 v166, 0x10800, v158
	s_mov_b64 s[10:11], -1
	s_mov_b32 s4, 0x3c800000
	v_add_u32_e32 v165, 0x23a00, v158
	v_add_u32_e32 v167, 0x23e00, v158
	v_add_u32_e32 v168, 0x24200, v158
	v_add_u32_e32 v169, 0x24600, v158
	v_add_u32_e32 v170, 0x24a00, v158
	v_add_u32_e32 v171, 0x24e00, v158
	v_add_u32_e32 v172, 0x25200, v158
	v_add_u32_e32 v173, 0x25600, v158
	v_add_u32_e32 v174, 0x21a00, v158
	v_add_u32_e32 v175, 0x21e00, v158
	v_add_u32_e32 v176, 0x22200, v158
	v_add_u32_e32 v177, 0x22600, v158
	v_add_u32_e32 v178, 0x22a00, v158
	v_add_u32_e32 v179, 0x22e00, v158
	v_add_u32_e32 v180, 0x23200, v158
	v_add_u32_e32 v181, 0x23600, v158
	s_mov_b32 s8, 0x3e8293ee
	s_mov_b32 s14, 0
	s_waitcnt vmcnt(0) lgkmcnt(0)
	s_barrier
